# speedup vs baseline: 1.0114x; 1.0107x over previous
_Z13logits_kernelPKDv8_DF16bS1_PKfS3_PDv2_fS5_Pf:
	s_load_dwordx4 s[4:7], s[0:1], 0x0
	s_load_dwordx4 s[12:15], s[0:1], 0x10
	s_load_dwordx4 s[24:27], s[0:1], 0x20
	s_load_dwordx2 s[28:29], s[0:1], 0x30
	s_lshl_b32 s3, s2, 1
	s_and_b32 s3, s3, 14
	s_ashr_i32 s8, s2, 7
	s_bfe_u32 s10, s2, 0x40003
	s_add_i32 s3, s3, s8
	s_and_b32 s23, s2, 7
	v_lshrrev_b32_e32 v1, 6, v0
	v_and_b32_e32 v2, 63, v0
	s_movk_i32 s11, 0x3000
	v_add_u32_e32 v6, s23, v1
	v_lshlrev_b32_e32 v2, 4, v2
	v_and_b32_e32 v6, 3, v6
	v_and_b32_e32 v5, 31, v0
	v_mad_u32_u24 v6, v6, s11, v2
	v_lshlrev_b32_e32 v5, 2, v5
	s_mul_i32 s9, s23, 11
	s_lshr_b32 s9, s9, 5
	s_mul_i32 s9, s9, 3
	s_sub_i32 s23, s23, s9
	s_add_i32 s9, s23, 1
	s_cmp_ge_u32 s9, 3
	s_cselect_b32 s30, 0, s9
	s_add_i32 s9, s30, 1
	s_cmp_ge_u32 s9, 3
	s_cselect_b32 s31, 0, s9
	s_lshl_b32 s23, s23, 12
	s_lshl_b32 s30, s30, 12
	s_lshl_b32 s31, s31, 12
	s_lshl_b32 s9, s3, 9
	v_add_u32_e32 v2, s23, v6
	v_add_u32_e32 v3, s30, v6
	v_add_u32_e32 v4, s31, v6
	v_add_u32_e32 v5, s9, v5
	s_mul_i32 s8, s10, 0xc000
	s_mul_i32 s9, s3, 0x30000
	s_waitcnt lgkmcnt(0)
	s_load_dword s22, s[14:15], 0x0
	v_readfirstlane_b32 s23, v0
	s_nop 0
	s_cmp_lg_u32 s23, 0
	s_cbranch_scc1 .Llg_nocnt
	global_load_dword v248, v5, s[12:13]
	global_load_dword v249, v5, s[12:13] offset:128
	global_load_dword v250, v5, s[12:13] offset:256
	global_load_dword v251, v5, s[12:13] offset:384
